# speedup vs baseline: 1.0638x; 1.0126x over previous
_Z12k_layer_pool9LayerArgs:
	s_load_dwordx8 s[4:11], s[0:1], 0x0
	s_load_dwordx8 s[12:19], s[0:1], 0x20
	s_load_dwordx2 s[22:23], s[0:1], 0x60
	s_load_dwordx2 s[30:31], s[0:1], 0x58
	v_and_b32_e32 v159, 63, v0
	v_lshrrev_b32_e32 v160, 6, v0
	v_and_b32_e32 v143, 3, v159
	v_and_b32_e32 v167, 15, v159
	s_nop 0
	v_readfirstlane_b32 s61, v160
	s_waitcnt lgkmcnt(0)
	s_mov_b64 s[26:27], s[6:7]
	s_mov_b64 s[28:29], s[10:11]
	s_mov_b64 s[24:25], s[14:15]
	s_mov_b64 s[64:65], s[16:17]
	s_mov_b64 s[66:67], s[18:19]
	s_mov_b64 s[68:69], s[8:9]
	s_mov_b32 s8, s4
	s_and_b32 s9, s5, 0xffff
	s_mov_b32 s10, 0x40000000
	s_mov_b32 s11, 0x20000
	s_mov_b32 s12, s68
	s_and_b32 s13, s69, 0xffff
	s_mov_b32 s14, 0x40000000
	s_mov_b32 s15, 0x20000
	s_add_u32 s16, s24, 0x712bd00
	s_addc_u32 s17, s25, 0
	s_add_u32 s18, s16, 0xc35000
	s_addc_u32 s19, s17, 0
	s_add_u32 s20, s16, 0x186a000
	s_addc_u32 s21, s17, 0
	s_mul_i32 s52, s2, 49
	s_mov_b32 s71, s52
	s_add_u32 s32, s52, 49
	s_min_u32 s32, s32, 12500
	s_mov_b32 s72, s61
	s_add_u32 s35, s52, s61
	s_mul_i32 s61, s61, 0x1100
	s_add_u32 s61, s61, 0x18000
	v_lshrrev_b32_e32 v160, 2, v159
	v_lshrrev_b32_e32 v161, 4, v159
	v_lshlrev_b32_e32 v134, 4, v143
	v_mov_b32_e32 v135, v134
	v_mul_u32_u24_e32 v162, 0x110, v160
	v_add3_u32 v136, v162, v134, s61
	v_mul_u32_u24_e32 v162, 0x110, v167
	v_lshl_add_u32 v137, v161, 4, v162
	v_add_u32_e32 v137, s61, v137
	v_lshl_add_u32 v140, v161, 3, v162
	v_add_u32_e32 v140, s61, v140
	v_mul_u32_u24_e32 v162, 0x110, v161
	v_lshl_add_u32 v141, v167, 4, v162
	v_add_u32_e32 v141, s61, v141
	v_lshlrev_b32_e32 v138, 4, v159
	v_add_u32_e32 v139, 0x10000, v138
	v_lshlrev_b32_e32 v142, 8, v161
	v_lshl_add_u32 v142, v167, 4, v142
	v_mov_b32_e32 v144, 0x800000
	v_lshlrev_b32_e32 v145, 2, v160
	v_lshl_add_u32 v145, v143, 6, v145
	v_mul_u32_u24_e32 v146, 0x100, v160
	v_add_u32_e32 v146, v146, v135
	s_lshl_b32 s52, s35, 10
	v_add_u32_e32 v160, s52, v145
	global_load_dword v151, v160, s[16:17]
	global_load_dword v152, v160, s[16:17] offset:256
	global_load_dword v153, v160, s[18:19]
	global_load_dword v154, v160, s[18:19] offset:256
	s_lshl_b32 s52, s35, 2
	v_and_b32_e32 v161, 1, v159
	v_mul_u32_u24_e32 v161, 0xc350, v161
	v_add_u32_e32 v161, s52, v161
	global_load_dword v155, v161, s[20:21]
	s_min_u32 s52, s35, 12499
	s_lshl_b32 s52, s52, 6
	v_lshl_add_u32 v161, v167, 2, s52
	global_load_dword v164, v161, s[30:31]
	s_mov_b32 s40, s64
	s_and_b32 s41, s65, 0xffff
	s_mov_b32 s42, 0x18000
	s_mov_b32 s43, 0x20000
	v_lshlrev_b32_e32 v160, 4, v0
	buffer_load_dwordx4 v[82:85], v160, s[40:43], 0 offen
	v_add_u32_e32 v161, 0x3000, v160
	buffer_load_dwordx4 v[86:89], v161, s[40:43], 0 offen
	v_add_u32_e32 v161, 0x6000, v160
	buffer_load_dwordx4 v[90:93], v161, s[40:43], 0 offen
	v_add_u32_e32 v161, 0x9000, v160
	buffer_load_dwordx4 v[94:97], v161, s[40:43], 0 offen
	v_add_u32_e32 v161, 0xc000, v160
	buffer_load_dwordx4 v[98:101], v161, s[40:43], 0 offen
	v_add_u32_e32 v161, 0xf000, v160
	buffer_load_dwordx4 v[102:105], v161, s[40:43], 0 offen
	v_add_u32_e32 v161, 0x12000, v160
	buffer_load_dwordx4 v[106:109], v161, s[40:43], 0 offen
	v_add_u32_e32 v161, 0x15000, v160
	buffer_load_dwordx4 v[110:113], v161, s[40:43], 0 offen
	v_lshlrev_b32_e32 v162, 2, v0
	v_cmp_gt_u32_e32 vcc, 0x80, v0
	s_and_saveexec_b64 s[58:59], vcc
	s_cbranch_execz .Lfp_nobias
	global_load_dword v163, v162, s[66:67]
.Lfp_nobias:
	s_mov_b64 exec, s[58:59]
	v_mov_b32_e32 v157, 0
	v_add_u32_e32 v158, 0x24e00, v162
	ds_write_b32 v158, v157
	v_cmp_gt_u32_e32 vcc, 0x100, v0
	s_and_saveexec_b64 s[58:59], vcc
	ds_write_b32 v158, v157 offset:3072
	s_mov_b64 exec, s[58:59]
	s_lshl_b32 s53, s71, 6
	s_load_dword s60, s[30:31], s53
	s_waitcnt vmcnt(8)
	s_mov_b32 s34, s35
	v_readlane_b32 s52, v155, 0
	v_readlane_b32 s53, v155, 1
	s_cmp_lt_u32 s34, s32
	s_cselect_b32 s47, s52, 0
	s_cselect_b32 s48, s53, 0
	s_max_u32 s38, s47, 2
	s_max_u32 s39, s48, 2
	v_cmp_gt_i32_e32 vcc, s47, v143
	s_nop 1
	v_cndmask_b32_e32 v147, v144, v151, vcc
	v_mov_b32_e32 v148, v152
	v_mov_b32_e32 v149, v153
	v_mov_b32_e32 v150, v154
	v_mov_b32_e32 v165, v164
	s_mov_b32 s44, 0
	s_mov_b32 s46, 0
	s_mov_b32 s45, s38
	s_mov_b64 s[40:41], s[8:9]
	s_mov_b64 s[42:43], s[10:11]
	s_movk_i32 s49, 0x100
	s_mov_b32 s70, 0
	s_add_u32 s35, s71, s72
	s_add_u32 s35, s35, 12
	s_lshl_b32 s52, s35, 10
	v_add_u32_e32 v160, s52, v145
	global_load_dword v151, v160, s[16:17]
	global_load_dword v152, v160, s[16:17] offset:256
	global_load_dword v153, v160, s[18:19]
	global_load_dword v154, v160, s[18:19] offset:256
	s_lshl_b32 s52, s35, 2
	v_and_b32_e32 v161, 1, v159
	v_mul_u32_u24_e32 v161, 0xc350, v161
	v_add_u32_e32 v161, s52, v161
	global_load_dword v155, v161, s[20:21]
	s_min_u32 s52, s35, 12499
	s_lshl_b32 s52, s52, 6
	v_lshl_add_u32 v161, v167, 2, s52
	global_load_dword v164, v161, s[30:31]
	s_mov_b32 s64, 2
	s_mov_b32 s66, 0
	s_branch .Lfp_st_0
.Lfp_postpro:
	s_waitcnt vmcnt(22)
	v_lshlrev_b32_e32 v160, 4, v0
	ds_write_b128 v160, v[82:85]
	v_add_u32_e32 v161, 0x3000, v160
	ds_write_b128 v161, v[86:89]
	v_add_u32_e32 v161, 0x6000, v160
	ds_write_b128 v161, v[90:93]
	v_add_u32_e32 v161, 0x9000, v160
	ds_write_b128 v161, v[94:97]
	v_add_u32_e32 v161, 0xc000, v160
	ds_write_b128 v161, v[98:101]
	v_add_u32_e32 v161, 0xf000, v160
	ds_write_b128 v161, v[102:105]
	v_add_u32_e32 v161, 0x12000, v160
	ds_write_b128 v161, v[106:109]
	v_add_u32_e32 v161, 0x15000, v160
	ds_write_b128 v161, v[110:113]
	v_cmp_gt_u32_e32 vcc, 0x80, v0
	s_and_saveexec_b64 s[58:59], vcc
	v_lshlrev_b32_e32 v162, 2, v0
	v_add_u32_e32 v162, 0x24c00, v162
	ds_write_b32 v162, v163
	s_mov_b64 exec, s[58:59]
	v_cmp_eq_u32_e32 vcc, 0, v0
	s_and_saveexec_b64 s[58:59], vcc
	v_mov_b32_e32 v160, 0x25e00
	s_add_u32 s53, s71, 24
	v_mov_b32_e32 v161, s53
	ds_write_b32 v160, v161
	s_mov_b64 exec, s[58:59]
	s_waitcnt lgkmcnt(0)
	s_barrier
	s_mov_b32 s64, 3
.Lfp_tilestart:
	s_mov_b32 s33, s34
	s_mov_b32 s65, s38
	s_mov_b32 s37, s39
	v_mov_b32_e32 v166, v165
	s_cmp_ge_u32 s33, s32
	s_cbranch_scc1 .Lfp_exit
	v_mov_b32_e32 v66, 0
	v_mov_b32_e32 v67, 0
	v_mov_b32_e32 v68, 0
	v_mov_b32_e32 v69, 0
	v_mov_b32_e32 v70, 0
	v_mov_b32_e32 v71, 0
	v_mov_b32_e32 v72, 0
	v_mov_b32_e32 v73, 0
	v_mov_b32_e32 v74, 0
	v_mov_b32_e32 v75, 0
	v_mov_b32_e32 v76, 0
	v_mov_b32_e32 v77, 0
	v_mov_b32_e32 v78, 0
	v_mov_b32_e32 v79, 0
	v_mov_b32_e32 v80, 0
	v_mov_b32_e32 v81, 0
	v_lshlrev_b32_e32 v163, 2, v167
	v_add_u32_e32 v163, 0x24c00, v163
	ds_read_b32 v82, v163 offset:0
	ds_read_b32 v86, v163 offset:64
	ds_read_b32 v90, v163 offset:128
	ds_read_b32 v94, v163 offset:192
	ds_read_b32 v98, v163 offset:256
	ds_read_b32 v102, v163 offset:320
	ds_read_b32 v106, v163 offset:384
	ds_read_b32 v110, v163 offset:448
	s_waitcnt lgkmcnt(0)
	v_mov_b32_e32 v83, v82
	v_mov_b32_e32 v84, v82
	v_mov_b32_e32 v85, v82
	v_mov_b32_e32 v87, v86
	v_mov_b32_e32 v88, v86
	v_mov_b32_e32 v89, v86
	v_mov_b32_e32 v91, v90
	v_mov_b32_e32 v92, v90
	v_mov_b32_e32 v93, v90
	v_mov_b32_e32 v95, v94
	v_mov_b32_e32 v96, v94
	v_mov_b32_e32 v97, v94
	v_mov_b32_e32 v99, v98
	v_mov_b32_e32 v100, v98
	v_mov_b32_e32 v101, v98
	v_mov_b32_e32 v103, v102
	v_mov_b32_e32 v104, v102
	v_mov_b32_e32 v105, v102
	v_mov_b32_e32 v107, v106
	v_mov_b32_e32 v108, v106
	v_mov_b32_e32 v109, v106
	v_mov_b32_e32 v111, v110
	v_mov_b32_e32 v112, v110
	v_mov_b32_e32 v113, v110
	s_cmp_eq_u32 s64, 3
	s_mov_b32 s64, 0
	s_cbranch_scc1 .Lfp_st_0
	s_cmp_eq_u32 s51, 0
	s_cbranch_scc1 .Lfp_is_0
	s_cmp_eq_u32 s51, 1
	s_cbranch_scc1 .Lfp_is_1
	s_cmp_eq_u32 s51, 2
	s_cbranch_scc1 .Lfp_is_2
	s_branch .Lfp_is_3

.Lfp_nx_3:
	s_cmp_eq_u32 s64, 2
	s_cbranch_scc1 .Lfp_postpro
	s_branch .Lfp_st_0

_Z10k_layer_fhILi96ELb1EEv9LayerArgsS0_i:
	s_movk_i32 s3, 0x58
	v_lshrrev_b32_e32 v133, 6, v0
	s_movk_i32 s4, 0x1100
	v_mov_b32_e32 v1, 0x18000
	v_mad_u32_u24 v1, v133, s4, v1
	s_mov_b64 s[4:5], -1
	s_waitcnt lgkmcnt(0)
	s_cmp_ge_i32 s2, s3
	v_lshlrev_b32_e32 v130, 4, v0
	s_cbranch_scc0 .LBB5_73
	s_load_dwordx8 s[4:11], s[0:1], 0x0
	s_load_dwordx8 s[12:19], s[0:1], 0x20
	s_load_dwordx2 s[22:23], s[0:1], 0x40
	v_and_b32_e32 v159, 63, v0
	v_lshrrev_b32_e32 v160, 6, v0
	v_and_b32_e32 v143, 3, v159
	v_and_b32_e32 v167, 15, v159
	s_nop 0
	v_readfirstlane_b32 s61, v160
	s_waitcnt lgkmcnt(0)
	s_mov_b64 s[26:27], s[6:7]
	s_mov_b64 s[28:29], s[10:11]
	s_mov_b64 s[24:25], s[14:15]
	s_mov_b64 s[64:65], s[16:17]
	s_mov_b64 s[66:67], s[18:19]
	s_mov_b64 s[68:69], s[8:9]
	s_mov_b32 s8, s4
	s_and_b32 s9, s5, 0xffff
	s_mov_b32 s10, 0x40000000
	s_mov_b32 s11, 0x20000
	s_mov_b32 s12, s68
	s_and_b32 s13, s69, 0xffff
	s_mov_b32 s14, 0x40000000
	s_mov_b32 s15, 0x20000
	s_add_u32 s16, s24, 0x712bd00
	s_addc_u32 s17, s25, 0
	s_add_u32 s18, s16, 0xc35000
	s_addc_u32 s19, s17, 0
	s_add_u32 s20, s16, 0x186a000
	s_addc_u32 s21, s17, 0
	s_sub_u32 s52, s2, 88
	s_mul_i32 s52, s52, 75
	s_mov_b32 s71, s52
	s_add_u32 s32, s52, 75
	s_min_u32 s32, s32, 12500
	s_mov_b32 s72, s61
	s_add_u32 s35, s52, s61
	s_mul_i32 s61, s61, 0x1100
	s_add_u32 s61, s61, 0x18000
	v_lshrrev_b32_e32 v160, 2, v159
	v_lshrrev_b32_e32 v161, 4, v159
	v_lshlrev_b32_e32 v134, 4, v143
	v_mov_b32_e32 v135, v134
	v_mul_u32_u24_e32 v162, 0x110, v160
	v_add3_u32 v136, v162, v134, s61
	v_mul_u32_u24_e32 v162, 0x110, v167
	v_lshl_add_u32 v137, v161, 4, v162
	v_add_u32_e32 v137, s61, v137
	v_lshl_add_u32 v140, v161, 3, v162
	v_add_u32_e32 v140, s61, v140
	v_mul_u32_u24_e32 v162, 0x110, v161
	v_lshl_add_u32 v141, v167, 4, v162
	v_add_u32_e32 v141, s61, v141
	v_lshlrev_b32_e32 v138, 4, v159
	v_add_u32_e32 v139, 0x10000, v138
	v_lshlrev_b32_e32 v142, 8, v161
	v_lshl_add_u32 v142, v167, 4, v142
	v_mov_b32_e32 v144, 0x800000
	v_lshlrev_b32_e32 v145, 2, v160
	v_lshl_add_u32 v145, v143, 6, v145
	v_mul_u32_u24_e32 v146, 0xc0, v160
	v_add_u32_e32 v146, v146, v135
	s_lshl_b32 s52, s35, 10
	v_add_u32_e32 v160, s52, v145
	global_load_dword v151, v160, s[16:17]
	global_load_dword v152, v160, s[16:17] offset:256
	global_load_dword v153, v160, s[18:19]
	global_load_dword v154, v160, s[18:19] offset:256
	s_lshl_b32 s52, s35, 2
	v_and_b32_e32 v161, 1, v159
	v_mul_u32_u24_e32 v161, 0xc350, v161
	v_add_u32_e32 v161, s52, v161
	global_load_dword v155, v161, s[20:21]
	s_mov_b32 s40, s64
	s_and_b32 s41, s65, 0xffff
	s_mov_b32 s42, 0x14000
	s_mov_b32 s43, 0x20000
	v_lshlrev_b32_e32 v160, 4, v0
	buffer_load_dwordx4 v[82:85], v160, s[40:43], 0 offen
	v_add_u32_e32 v161, 0x3000, v160
	buffer_load_dwordx4 v[86:89], v161, s[40:43], 0 offen
	v_add_u32_e32 v161, 0x6000, v160
	buffer_load_dwordx4 v[90:93], v161, s[40:43], 0 offen
	v_add_u32_e32 v161, 0x9000, v160
	buffer_load_dwordx4 v[94:97], v161, s[40:43], 0 offen
	v_add_u32_e32 v161, 0xc000, v160
	buffer_load_dwordx4 v[98:101], v161, s[40:43], 0 offen
	v_add_u32_e32 v161, 0xf000, v160
	buffer_load_dwordx4 v[102:105], v161, s[40:43], 0 offen
	v_add_u32_e32 v161, 0x12000, v160
	buffer_load_dwordx4 v[106:109], v161, s[40:43], 0 offen
	v_lshlrev_b32_e32 v162, 2, v0
	v_cmp_gt_u32_e32 vcc, 0x80, v0
	s_and_saveexec_b64 s[58:59], vcc
	s_cbranch_execz .Lfa_nobias
	global_load_dword v163, v162, s[66:67]
.Lfa_nobias:
	s_mov_b64 exec, s[58:59]
	s_waitcnt vmcnt(7)
	s_mov_b32 s34, s35
	v_readlane_b32 s52, v155, 0
	v_readlane_b32 s53, v155, 1
	s_cmp_lt_u32 s34, s32
	s_cselect_b32 s47, s52, 0
	s_cselect_b32 s48, s53, 0
	s_max_u32 s38, s47, 2
	s_max_u32 s39, s48, 2
	v_cmp_gt_i32_e32 vcc, s47, v143
	s_nop 1
	v_cndmask_b32_e32 v147, v144, v151, vcc
	v_mov_b32_e32 v148, v152
	v_mov_b32_e32 v149, v153
	v_mov_b32_e32 v150, v154
	s_mov_b32 s44, 0
	s_mov_b32 s46, 0
	s_mov_b32 s45, s38
	s_mov_b64 s[40:41], s[8:9]
	s_mov_b64 s[42:43], s[10:11]
	s_movk_i32 s49, 0x100
	s_mov_b32 s70, 0
	s_add_u32 s35, s71, s72
	s_add_u32 s35, s35, 12
	s_lshl_b32 s52, s35, 10
	v_add_u32_e32 v160, s52, v145
	global_load_dword v151, v160, s[16:17]
	global_load_dword v152, v160, s[16:17] offset:256
	global_load_dword v153, v160, s[18:19]
	global_load_dword v154, v160, s[18:19] offset:256
	s_lshl_b32 s52, s35, 2
	v_and_b32_e32 v161, 1, v159
	v_mul_u32_u24_e32 v161, 0xc350, v161
	v_add_u32_e32 v161, s52, v161
	global_load_dword v155, v161, s[20:21]
	s_mov_b32 s64, 2
	s_mov_b32 s66, 0
	s_branch .Lfa_st_0
.Lfa_postpro:
	s_waitcnt vmcnt(21)
	v_lshlrev_b32_e32 v160, 4, v0
	ds_write_b128 v160, v[82:85]
	v_add_u32_e32 v161, 0x3000, v160
	ds_write_b128 v161, v[86:89]
	v_add_u32_e32 v161, 0x6000, v160
	ds_write_b128 v161, v[90:93]
	v_add_u32_e32 v161, 0x9000, v160
	ds_write_b128 v161, v[94:97]
	v_add_u32_e32 v161, 0xc000, v160
	ds_write_b128 v161, v[98:101]
	v_add_u32_e32 v161, 0xf000, v160
	ds_write_b128 v161, v[102:105]
	v_add_u32_e32 v161, 0x12000, v160
	ds_write_b128 v161, v[106:109]
	v_cmp_gt_u32_e32 vcc, 0x80, v0
	s_and_saveexec_b64 s[58:59], vcc
	v_lshlrev_b32_e32 v162, 2, v0
	v_add_u32_e32 v162, 0x24c00, v162
	ds_write_b32 v162, v163
	s_mov_b64 exec, s[58:59]
	v_cmp_eq_u32_e32 vcc, 0, v0
	s_and_saveexec_b64 s[58:59], vcc
	v_mov_b32_e32 v160, 0x24e00
	s_add_u32 s53, s71, 24
	v_mov_b32_e32 v161, s53
	ds_write_b32 v160, v161
	s_mov_b64 exec, s[58:59]
	s_waitcnt lgkmcnt(0)
	s_barrier
	s_mov_b32 s64, 3
.Lfa_tilestart:
	s_mov_b32 s33, s34
	s_mov_b32 s65, s38
	s_mov_b32 s37, s39
	s_cmp_ge_u32 s33, s32
	s_cbranch_scc1 .Lfa_exit
	v_mov_b32_e32 v66, 0
	v_mov_b32_e32 v67, 0
	v_mov_b32_e32 v68, 0
	v_mov_b32_e32 v69, 0
	v_mov_b32_e32 v70, 0
	v_mov_b32_e32 v71, 0
	v_mov_b32_e32 v72, 0
	v_mov_b32_e32 v73, 0
	v_mov_b32_e32 v74, 0
	v_mov_b32_e32 v75, 0
	v_mov_b32_e32 v76, 0
	v_mov_b32_e32 v77, 0
	v_mov_b32_e32 v78, 0
	v_mov_b32_e32 v79, 0
	v_mov_b32_e32 v80, 0
	v_mov_b32_e32 v81, 0
	v_lshrrev_b32_e32 v163, 4, v159
	v_lshlrev_b32_e32 v163, 4, v163
	v_add_u32_e32 v163, 0x24c00, v163
	ds_read_b128 v[82:85], v163 offset:0
	ds_read_b128 v[86:89], v163 offset:64
	ds_read_b128 v[90:93], v163 offset:128
	ds_read_b128 v[94:97], v163 offset:192
	ds_read_b128 v[98:101], v163 offset:256
	ds_read_b128 v[102:105], v163 offset:320
	ds_read_b128 v[106:109], v163 offset:384
	ds_read_b128 v[110:113], v163 offset:448
	s_waitcnt lgkmcnt(0)
	s_cmp_eq_u32 s64, 3
	s_mov_b32 s64, 0
	s_cbranch_scc1 .Lfa_st_0
	s_cmp_eq_u32 s51, 0
	s_cbranch_scc1 .Lfa_is_0
	s_cmp_eq_u32 s51, 1
	s_cbranch_scc1 .Lfa_is_1
	s_cmp_eq_u32 s51, 2
	s_cbranch_scc1 .Lfa_is_2
	s_branch .Lfa_is_3

_Z10k_layer_fhILi128ELb1EEv9LayerArgsS0_i:
	s_movk_i32 s3, 0x58
	v_lshrrev_b32_e32 v138, 6, v0
	s_movk_i32 s4, 0x1100
	v_mov_b32_e32 v1, 0x18000
	v_mad_u32_u24 v1, v138, s4, v1
	s_mov_b64 s[4:5], -1
	s_waitcnt lgkmcnt(0)
	s_cmp_ge_i32 s2, s3
	v_lshlrev_b32_e32 v130, 4, v0
	s_cbranch_scc0 .LBB6_69
	s_load_dwordx8 s[4:11], s[0:1], 0x0
	s_load_dwordx8 s[12:19], s[0:1], 0x20
	s_load_dwordx2 s[22:23], s[0:1], 0x40
	v_and_b32_e32 v159, 63, v0
	v_lshrrev_b32_e32 v160, 6, v0
	v_and_b32_e32 v143, 3, v159
	v_and_b32_e32 v167, 15, v159
	s_nop 0
	v_readfirstlane_b32 s61, v160
	s_waitcnt lgkmcnt(0)
	s_mov_b64 s[26:27], s[6:7]
	s_mov_b64 s[28:29], s[10:11]
	s_mov_b64 s[24:25], s[14:15]
	s_mov_b64 s[64:65], s[16:17]
	s_mov_b64 s[66:67], s[18:19]
	s_mov_b64 s[68:69], s[8:9]
	s_mov_b32 s8, s4
	s_and_b32 s9, s5, 0xffff
	s_mov_b32 s10, 0x40000000
	s_mov_b32 s11, 0x20000
	s_mov_b32 s12, s68
	s_and_b32 s13, s69, 0xffff
	s_mov_b32 s14, 0x40000000
	s_mov_b32 s15, 0x20000
	s_add_u32 s16, s24, 0x712bd00
	s_addc_u32 s17, s25, 0
	s_add_u32 s18, s16, 0xc35000
	s_addc_u32 s19, s17, 0
	s_add_u32 s20, s16, 0x186a000
	s_addc_u32 s21, s17, 0
	s_sub_u32 s52, s2, 88
	s_mul_i32 s52, s52, 75
	s_mov_b32 s71, s52
	s_add_u32 s32, s52, 75
	s_min_u32 s32, s32, 12500
	s_mov_b32 s72, s61
	s_add_u32 s35, s52, s61
	s_mul_i32 s61, s61, 0x1100
	s_add_u32 s61, s61, 0x18000
	v_lshrrev_b32_e32 v160, 2, v159
	v_lshrrev_b32_e32 v161, 4, v159
	v_lshlrev_b32_e32 v134, 4, v143
	v_mov_b32_e32 v135, v134
	v_mul_u32_u24_e32 v162, 0x110, v160
	v_add3_u32 v136, v162, v134, s61
	v_mul_u32_u24_e32 v162, 0x110, v167
	v_lshl_add_u32 v137, v161, 4, v162
	v_add_u32_e32 v137, s61, v137
	v_lshl_add_u32 v140, v161, 3, v162
	v_add_u32_e32 v140, s61, v140
	v_mul_u32_u24_e32 v162, 0x110, v161
	v_lshl_add_u32 v141, v167, 4, v162
	v_add_u32_e32 v141, s61, v141
	v_lshlrev_b32_e32 v138, 4, v159
	v_add_u32_e32 v139, 0x10000, v138
	v_lshlrev_b32_e32 v142, 8, v161
	v_lshl_add_u32 v142, v167, 4, v142
	v_mov_b32_e32 v144, 0x800000
	v_lshlrev_b32_e32 v145, 2, v160
	v_lshl_add_u32 v145, v143, 6, v145
	v_mul_u32_u24_e32 v146, 0x100, v160
	v_add_u32_e32 v146, v146, v135
	s_lshl_b32 s52, s35, 10
	v_add_u32_e32 v160, s52, v145
	global_load_dword v151, v160, s[16:17]
	global_load_dword v152, v160, s[16:17] offset:256
	global_load_dword v153, v160, s[18:19]
	global_load_dword v154, v160, s[18:19] offset:256
	s_lshl_b32 s52, s35, 2
	v_and_b32_e32 v161, 1, v159
	v_mul_u32_u24_e32 v161, 0xc350, v161
	v_add_u32_e32 v161, s52, v161
	global_load_dword v155, v161, s[20:21]
	s_mov_b32 s40, s64
	s_and_b32 s41, s65, 0xffff
	s_mov_b32 s42, 0x18000
	s_mov_b32 s43, 0x20000
	v_lshlrev_b32_e32 v160, 4, v0
	buffer_load_dwordx4 v[82:85], v160, s[40:43], 0 offen
	v_add_u32_e32 v161, 0x3000, v160
	buffer_load_dwordx4 v[86:89], v161, s[40:43], 0 offen
	v_add_u32_e32 v161, 0x6000, v160
	buffer_load_dwordx4 v[90:93], v161, s[40:43], 0 offen
	v_add_u32_e32 v161, 0x9000, v160
	buffer_load_dwordx4 v[94:97], v161, s[40:43], 0 offen
	v_add_u32_e32 v161, 0xc000, v160
	buffer_load_dwordx4 v[98:101], v161, s[40:43], 0 offen
	v_add_u32_e32 v161, 0xf000, v160
	buffer_load_dwordx4 v[102:105], v161, s[40:43], 0 offen
	v_add_u32_e32 v161, 0x12000, v160
	buffer_load_dwordx4 v[106:109], v161, s[40:43], 0 offen
	v_add_u32_e32 v161, 0x15000, v160
	buffer_load_dwordx4 v[110:113], v161, s[40:43], 0 offen
	v_lshlrev_b32_e32 v162, 2, v0
	v_cmp_gt_u32_e32 vcc, 0x80, v0
	s_and_saveexec_b64 s[58:59], vcc
	s_cbranch_execz .Lfb_nobias
	global_load_dword v163, v162, s[66:67]
.Lfb_nobias:
	s_mov_b64 exec, s[58:59]
	s_waitcnt vmcnt(8)
	s_mov_b32 s34, s35
	v_readlane_b32 s52, v155, 0
	v_readlane_b32 s53, v155, 1
	s_cmp_lt_u32 s34, s32
	s_cselect_b32 s47, s52, 0
	s_cselect_b32 s48, s53, 0
	s_max_u32 s38, s47, 2
	s_max_u32 s39, s48, 2
	v_cmp_gt_i32_e32 vcc, s47, v143
	s_nop 1
	v_cndmask_b32_e32 v147, v144, v151, vcc
	v_mov_b32_e32 v148, v152
	v_mov_b32_e32 v149, v153
	v_mov_b32_e32 v150, v154
	s_mov_b32 s44, 0
	s_mov_b32 s46, 0
	s_mov_b32 s45, s38
	s_mov_b64 s[40:41], s[8:9]
	s_mov_b64 s[42:43], s[10:11]
	s_movk_i32 s49, 0x100
	s_mov_b32 s70, 0
	s_add_u32 s35, s71, s72
	s_add_u32 s35, s35, 12
	s_lshl_b32 s52, s35, 10
	v_add_u32_e32 v160, s52, v145
	global_load_dword v151, v160, s[16:17]
	global_load_dword v152, v160, s[16:17] offset:256
	global_load_dword v153, v160, s[18:19]
	global_load_dword v154, v160, s[18:19] offset:256
	s_lshl_b32 s52, s35, 2
	v_and_b32_e32 v161, 1, v159
	v_mul_u32_u24_e32 v161, 0xc350, v161
	v_add_u32_e32 v161, s52, v161
	global_load_dword v155, v161, s[20:21]
	s_mov_b32 s64, 2
	s_mov_b32 s66, 0
	s_branch .Lfb_st_0
.Lfb_postpro:
	s_waitcnt vmcnt(21)
	v_lshlrev_b32_e32 v160, 4, v0
	ds_write_b128 v160, v[82:85]
	v_add_u32_e32 v161, 0x3000, v160
	ds_write_b128 v161, v[86:89]
	v_add_u32_e32 v161, 0x6000, v160
	ds_write_b128 v161, v[90:93]
	v_add_u32_e32 v161, 0x9000, v160
	ds_write_b128 v161, v[94:97]
	v_add_u32_e32 v161, 0xc000, v160
	ds_write_b128 v161, v[98:101]
	v_add_u32_e32 v161, 0xf000, v160
	ds_write_b128 v161, v[102:105]
	v_add_u32_e32 v161, 0x12000, v160
	ds_write_b128 v161, v[106:109]
	v_add_u32_e32 v161, 0x15000, v160
	ds_write_b128 v161, v[110:113]
	v_cmp_gt_u32_e32 vcc, 0x80, v0
	s_and_saveexec_b64 s[58:59], vcc
	v_lshlrev_b32_e32 v162, 2, v0
	v_add_u32_e32 v162, 0x24c00, v162
	ds_write_b32 v162, v163
	s_mov_b64 exec, s[58:59]
	v_cmp_eq_u32_e32 vcc, 0, v0
	s_and_saveexec_b64 s[58:59], vcc
	v_mov_b32_e32 v160, 0x24e00
	s_add_u32 s53, s71, 24
	v_mov_b32_e32 v161, s53
	ds_write_b32 v160, v161
	s_mov_b64 exec, s[58:59]
	s_waitcnt lgkmcnt(0)
	s_barrier
	s_mov_b32 s64, 3
